# speedup vs baseline: 1.0224x; 1.0050x over previous
.LBB0_40:
	s_or_b64 exec, exec, s[6:7]
	v_cmp_gt_u32_e32 vcc, 16, v2
	s_and_b64 s[6:7], s[18:19], vcc
	s_and_saveexec_b64 s[4:5], s[6:7]
	v_lshlrev_b32_e32 v2, 2, v2
	v_or_b32_e32 v1, 7, v1
	ds_write_b32 v2, v1
	s_or_b64 exec, exec, s[4:5]
	v_mov_b32_e32 v35, 0
	s_waitcnt lgkmcnt(0)
	s_barrier
	ds_read_b128 v[2:5], v35
	ds_read_b128 v[6:9], v35 offset:16
	ds_read_b128 v[10:13], v35 offset:32
	ds_read_b128 v[14:17], v35 offset:48
	s_and_b64 s[4:5], s[30:31], exec
	s_cselect_b32 s9, s25, s27
	s_cselect_b32 s8, s24, s26
	s_cselect_b32 s11, s21, s23
	s_cselect_b32 s10, s20, s22
	s_lshl_b32 s6, s36, 23
	s_add_u32 s8, s8, s6
	s_addc_u32 s9, s9, 0
	s_or_b32 s6, s34, s33
	s_mulk_i32 s6, 0x880
	s_add_u32 s10, s10, s6
	s_addc_u32 s11, s11, 0
	v_lshlrev_b32_e32 v1, 4, v0
	v_lshlrev_b32_e32 v66, 3, v0
	s_waitcnt lgkmcnt(0)
	v_readfirstlane_b32 s40, v2
	v_readfirstlane_b32 s41, v3
	v_readfirstlane_b32 s42, v4
	v_readfirstlane_b32 s43, v5
	v_readfirstlane_b32 s44, v6
	v_readfirstlane_b32 s45, v7
	v_readfirstlane_b32 s46, v8
	v_readfirstlane_b32 s47, v9
	v_readfirstlane_b32 s48, v10
	v_readfirstlane_b32 s49, v11
	v_readfirstlane_b32 s50, v12
	v_readfirstlane_b32 s51, v13
	v_readfirstlane_b32 s52, v14
	v_readfirstlane_b32 s53, v15
	v_readfirstlane_b32 s54, v16
	v_readfirstlane_b32 s55, v17
	s_max_i32 s12, s40, 0
	s_lshl_b32 s12, s12, 12
	s_add_u32 s12, s8, s12
	s_addc_u32 s13, s9, 0
	global_load_dwordx4 v[2:5], v1, s[12:13] nt
	s_max_i32 s12, s41, 0
	s_lshl_b32 s12, s12, 12
	s_add_u32 s12, s8, s12
	s_addc_u32 s13, s9, 0
	global_load_dwordx4 v[6:9], v1, s[12:13] nt
	s_max_i32 s12, s42, 0
	s_lshl_b32 s12, s12, 12
	s_add_u32 s12, s8, s12
	s_addc_u32 s13, s9, 0
	global_load_dwordx4 v[10:13], v1, s[12:13] nt
	s_max_i32 s12, s43, 0
	s_lshl_b32 s12, s12, 12
	s_add_u32 s12, s8, s12
	s_addc_u32 s13, s9, 0
	global_load_dwordx4 v[14:17], v1, s[12:13] nt
	s_max_i32 s12, s44, 0
	s_lshl_b32 s12, s12, 12
	s_add_u32 s12, s8, s12
	s_addc_u32 s13, s9, 0
	global_load_dwordx4 v[18:21], v1, s[12:13] nt
	s_max_i32 s12, s45, 0
	s_lshl_b32 s12, s12, 12
	s_add_u32 s12, s8, s12
	s_addc_u32 s13, s9, 0
	global_load_dwordx4 v[22:25], v1, s[12:13] nt
	s_max_i32 s12, s46, 0
	s_lshl_b32 s12, s12, 12
	s_add_u32 s12, s8, s12
	s_addc_u32 s13, s9, 0
	global_load_dwordx4 v[26:29], v1, s[12:13] nt
	s_max_i32 s12, s47, 0
	s_lshl_b32 s12, s12, 12
	s_add_u32 s12, s8, s12
	s_addc_u32 s13, s9, 0
	global_load_dwordx4 v[30:33], v1, s[12:13] nt
	s_max_i32 s12, s48, 0
	s_lshl_b32 s12, s12, 12
	s_add_u32 s12, s8, s12
	s_addc_u32 s13, s9, 0
	global_load_dwordx4 v[34:37], v1, s[12:13] nt
	s_max_i32 s12, s49, 0
	s_lshl_b32 s12, s12, 12
	s_add_u32 s12, s8, s12
	s_addc_u32 s13, s9, 0
	global_load_dwordx4 v[38:41], v1, s[12:13] nt
	s_max_i32 s12, s50, 0
	s_lshl_b32 s12, s12, 12
	s_add_u32 s12, s8, s12
	s_addc_u32 s13, s9, 0
	global_load_dwordx4 v[42:45], v1, s[12:13] nt
	s_max_i32 s12, s51, 0
	s_lshl_b32 s12, s12, 12
	s_add_u32 s12, s8, s12
	s_addc_u32 s13, s9, 0
	global_load_dwordx4 v[46:49], v1, s[12:13] nt
	s_max_i32 s12, s52, 0
	s_lshl_b32 s12, s12, 12
	s_add_u32 s12, s8, s12
	s_addc_u32 s13, s9, 0
	global_load_dwordx4 v[50:53], v1, s[12:13] nt
	s_max_i32 s12, s53, 0
	s_lshl_b32 s12, s12, 12
	s_add_u32 s12, s8, s12
	s_addc_u32 s13, s9, 0
	global_load_dwordx4 v[54:57], v1, s[12:13] nt
	s_max_i32 s12, s54, 0
	s_lshl_b32 s12, s12, 12
	s_add_u32 s12, s8, s12
	s_addc_u32 s13, s9, 0
	global_load_dwordx4 v[58:61], v1, s[12:13] nt
	s_max_i32 s12, s55, 0
	s_lshl_b32 s12, s12, 12
	s_add_u32 s12, s8, s12
	s_addc_u32 s13, s9, 0
	global_load_dwordx4 v[62:65], v1, s[12:13] nt
	s_waitcnt vmcnt(14)
	s_cmp_lt_i32 s40, 0
	s_cselect_b32 s14, 0, -1
	v_cvt_pk_f16_f32 v2, v2, v3
	v_cvt_pk_f16_f32 v3, v4, v5
	v_and_b32_e32 v2, s14, v2
	v_and_b32_e32 v3, s14, v3
	global_store_dwordx2 v66, v[2:3], s[10:11] sc0 sc1
	s_cmp_lt_i32 s41, 0
	s_cselect_b32 s14, 0, -1
	v_cvt_pk_f16_f32 v6, v6, v7
	v_cvt_pk_f16_f32 v7, v8, v9
	v_and_b32_e32 v6, s14, v6
	v_and_b32_e32 v7, s14, v7
	global_store_dwordx2 v66, v[6:7], s[10:11] offset:2176 sc0 sc1
	s_add_u32 s10, s10, 0x1100
	s_addc_u32 s11, s11, 0
	s_waitcnt vmcnt(14)
	s_cmp_lt_i32 s42, 0
	s_cselect_b32 s14, 0, -1
	v_cvt_pk_f16_f32 v10, v10, v11
	v_cvt_pk_f16_f32 v11, v12, v13
	v_and_b32_e32 v10, s14, v10
	v_and_b32_e32 v11, s14, v11
	global_store_dwordx2 v66, v[10:11], s[10:11] sc0 sc1
	s_cmp_lt_i32 s43, 0
	s_cselect_b32 s14, 0, -1
	v_cvt_pk_f16_f32 v14, v14, v15
	v_cvt_pk_f16_f32 v15, v16, v17
	v_and_b32_e32 v14, s14, v14
	v_and_b32_e32 v15, s14, v15
	global_store_dwordx2 v66, v[14:15], s[10:11] offset:2176 sc0 sc1
	s_add_u32 s10, s10, 0x1100
	s_addc_u32 s11, s11, 0
	s_waitcnt vmcnt(14)
	s_cmp_lt_i32 s44, 0
	s_cselect_b32 s14, 0, -1
	v_cvt_pk_f16_f32 v18, v18, v19
	v_cvt_pk_f16_f32 v19, v20, v21
	v_and_b32_e32 v18, s14, v18
	v_and_b32_e32 v19, s14, v19
	global_store_dwordx2 v66, v[18:19], s[10:11] sc0 sc1
	s_cmp_lt_i32 s45, 0
	s_cselect_b32 s14, 0, -1
	v_cvt_pk_f16_f32 v22, v22, v23
	v_cvt_pk_f16_f32 v23, v24, v25
	v_and_b32_e32 v22, s14, v22
	v_and_b32_e32 v23, s14, v23
	global_store_dwordx2 v66, v[22:23], s[10:11] offset:2176 sc0 sc1
	s_add_u32 s10, s10, 0x1100
	s_addc_u32 s11, s11, 0
	s_waitcnt vmcnt(14)
	s_cmp_lt_i32 s46, 0
	s_cselect_b32 s14, 0, -1
	v_cvt_pk_f16_f32 v26, v26, v27
	v_cvt_pk_f16_f32 v27, v28, v29
	v_and_b32_e32 v26, s14, v26
	v_and_b32_e32 v27, s14, v27
	global_store_dwordx2 v66, v[26:27], s[10:11] sc0 sc1
	s_cmp_lt_i32 s47, 0
	s_cselect_b32 s14, 0, -1
	v_cvt_pk_f16_f32 v30, v30, v31
	v_cvt_pk_f16_f32 v31, v32, v33
	v_and_b32_e32 v30, s14, v30
	v_and_b32_e32 v31, s14, v31
	global_store_dwordx2 v66, v[30:31], s[10:11] offset:2176 sc0 sc1
	s_add_u32 s10, s10, 0x1100
	s_addc_u32 s11, s11, 0
	s_waitcnt vmcnt(14)
	s_cmp_lt_i32 s48, 0
	s_cselect_b32 s14, 0, -1
	v_cvt_pk_f16_f32 v34, v34, v35
	v_cvt_pk_f16_f32 v35, v36, v37
	v_and_b32_e32 v34, s14, v34
	v_and_b32_e32 v35, s14, v35
	global_store_dwordx2 v66, v[34:35], s[10:11] sc0 sc1
	s_cmp_lt_i32 s49, 0
	s_cselect_b32 s14, 0, -1
	v_cvt_pk_f16_f32 v38, v38, v39
	v_cvt_pk_f16_f32 v39, v40, v41
	v_and_b32_e32 v38, s14, v38
	v_and_b32_e32 v39, s14, v39
	global_store_dwordx2 v66, v[38:39], s[10:11] offset:2176 sc0 sc1
	s_add_u32 s10, s10, 0x1100
	s_addc_u32 s11, s11, 0
	s_waitcnt vmcnt(14)
	s_cmp_lt_i32 s50, 0
	s_cselect_b32 s14, 0, -1
	v_cvt_pk_f16_f32 v42, v42, v43
	v_cvt_pk_f16_f32 v43, v44, v45
	v_and_b32_e32 v42, s14, v42
	v_and_b32_e32 v43, s14, v43
	global_store_dwordx2 v66, v[42:43], s[10:11] sc0 sc1
	s_cmp_lt_i32 s51, 0
	s_cselect_b32 s14, 0, -1
	v_cvt_pk_f16_f32 v46, v46, v47
	v_cvt_pk_f16_f32 v47, v48, v49
	v_and_b32_e32 v46, s14, v46
	v_and_b32_e32 v47, s14, v47
	global_store_dwordx2 v66, v[46:47], s[10:11] offset:2176 sc0 sc1
	s_add_u32 s10, s10, 0x1100
	s_addc_u32 s11, s11, 0
	s_waitcnt vmcnt(14)
	s_cmp_lt_i32 s52, 0
	s_cselect_b32 s14, 0, -1
	v_cvt_pk_f16_f32 v50, v50, v51
	v_cvt_pk_f16_f32 v51, v52, v53
	v_and_b32_e32 v50, s14, v50
	v_and_b32_e32 v51, s14, v51
	global_store_dwordx2 v66, v[50:51], s[10:11] sc0 sc1
	s_cmp_lt_i32 s53, 0
	s_cselect_b32 s14, 0, -1
	v_cvt_pk_f16_f32 v54, v54, v55
	v_cvt_pk_f16_f32 v55, v56, v57
	v_and_b32_e32 v54, s14, v54
	v_and_b32_e32 v55, s14, v55
	global_store_dwordx2 v66, v[54:55], s[10:11] offset:2176 sc0 sc1
	s_add_u32 s10, s10, 0x1100
	s_addc_u32 s11, s11, 0
	s_waitcnt vmcnt(14)
	s_cmp_lt_i32 s54, 0
	s_cselect_b32 s14, 0, -1
	v_cvt_pk_f16_f32 v58, v58, v59
	v_cvt_pk_f16_f32 v59, v60, v61
	v_and_b32_e32 v58, s14, v58
	v_and_b32_e32 v59, s14, v59
	global_store_dwordx2 v66, v[58:59], s[10:11] sc0 sc1
	s_cmp_lt_i32 s55, 0
	s_cselect_b32 s14, 0, -1
	v_cvt_pk_f16_f32 v62, v62, v63
	v_cvt_pk_f16_f32 v63, v64, v65
	v_and_b32_e32 v62, s14, v62
	v_and_b32_e32 v63, s14, v63
	global_store_dwordx2 v66, v[62:63], s[10:11] offset:2176 sc0 sc1
	s_endpgm
